# baseline (speedup 1.0000x reference)
.Lpc_anchor:
	s_add_u32 s44, s44, _Z7dog_finPKfS0_Pf-.Lpc_anchor
	s_addc_u32 s45, s45, 0
	s_load_dwordx16 s[48:63], s[44:45], 0x0
	s_load_dwordx16 s[64:79], s[44:45], 0x40
	s_load_dwordx16 s[80:95], s[44:45], 0x80
	v_mul_f32_e32 v16, v12, v12
	v_add_f32_e32 v17, 0x3f800000, v12
	v_add_f32_e32 v18, 0x40000000, v12
	v_add_f32_e32 v19, 0x40400000, v12
	v_mul_f32_e32 v17, v17, v17
	v_mul_f32_e32 v18, v18, v18
	v_mul_f32_e32 v19, v19, v19
	v_mul_f32_e32 v20, v8, v16
	v_mul_f32_e32 v24, v9, v16
	v_mul_f32_e32 v21, v8, v17
	v_mul_f32_e32 v25, v9, v17
	v_mul_f32_e32 v22, v8, v18
	v_mul_f32_e32 v26, v9, v18
	v_mul_f32_e32 v23, v8, v19
	v_mul_f32_e32 v27, v9, v19
	v_exp_f32_e32 v20, v20
	v_exp_f32_e32 v21, v21
	v_exp_f32_e32 v22, v22
	v_exp_f32_e32 v23, v23
	v_exp_f32_e32 v24, v24
	v_exp_f32_e32 v25, v25
	v_exp_f32_e32 v26, v26
	v_exp_f32_e32 v27, v27
	v_cvt_pk_f16_f32 v32, v20, v21
	v_cvt_pk_f16_f32 v33, v22, v23
	v_cvt_pk_f16_f32 v64, v24, v25
	v_cvt_pk_f16_f32 v65, v26, v27
	v_add_f32_e32 v16, 0x40800000, v12
	v_add_f32_e32 v17, 0x40a00000, v12
	v_add_f32_e32 v18, 0x40c00000, v12
	v_add_f32_e32 v19, 0x40e00000, v12
	v_mul_f32_e32 v16, v16, v16
	v_mul_f32_e32 v17, v17, v17
	v_mul_f32_e32 v18, v18, v18
	v_mul_f32_e32 v19, v19, v19
	v_mul_f32_e32 v20, v8, v16
	v_mul_f32_e32 v24, v9, v16
	v_mul_f32_e32 v21, v8, v17
	v_mul_f32_e32 v25, v9, v17
	v_mul_f32_e32 v22, v8, v18
	v_mul_f32_e32 v26, v9, v18
	v_mul_f32_e32 v23, v8, v19
	v_mul_f32_e32 v27, v9, v19
	v_exp_f32_e32 v20, v20
	v_exp_f32_e32 v21, v21
	v_exp_f32_e32 v22, v22
	v_exp_f32_e32 v23, v23
	v_exp_f32_e32 v24, v24
	v_exp_f32_e32 v25, v25
	v_exp_f32_e32 v26, v26
	v_exp_f32_e32 v27, v27
	v_cvt_pk_f16_f32 v34, v20, v21
	v_cvt_pk_f16_f32 v35, v22, v23
	v_cvt_pk_f16_f32 v66, v24, v25
	v_cvt_pk_f16_f32 v67, v26, v27
	v_add_f32_e32 v16, 0x42000000, v12
	v_add_f32_e32 v17, 0x42040000, v12
	v_add_f32_e32 v18, 0x42080000, v12
	v_add_f32_e32 v19, 0x420c0000, v12
	v_mul_f32_e32 v16, v16, v16
	v_mul_f32_e32 v17, v17, v17
	v_mul_f32_e32 v18, v18, v18
	v_mul_f32_e32 v19, v19, v19
	v_mul_f32_e32 v20, v8, v16
	v_mul_f32_e32 v24, v9, v16
	v_mul_f32_e32 v21, v8, v17
	v_mul_f32_e32 v25, v9, v17
	v_mul_f32_e32 v22, v8, v18
	v_mul_f32_e32 v26, v9, v18
	v_mul_f32_e32 v23, v8, v19
	v_mul_f32_e32 v27, v9, v19
	v_exp_f32_e32 v20, v20
	v_exp_f32_e32 v21, v21
	v_exp_f32_e32 v22, v22
	v_exp_f32_e32 v23, v23
	v_exp_f32_e32 v24, v24
	v_exp_f32_e32 v25, v25
	v_exp_f32_e32 v26, v26
	v_exp_f32_e32 v27, v27
	v_cvt_pk_f16_f32 v36, v20, v21
	v_cvt_pk_f16_f32 v37, v22, v23
	v_cvt_pk_f16_f32 v68, v24, v25
	v_cvt_pk_f16_f32 v69, v26, v27
	v_add_f32_e32 v16, 0x42100000, v12
	v_add_f32_e32 v17, 0x42140000, v12
	v_add_f32_e32 v18, 0x42180000, v12
	v_add_f32_e32 v19, 0x421c0000, v12
	v_mul_f32_e32 v16, v16, v16
	v_mul_f32_e32 v17, v17, v17
	v_mul_f32_e32 v18, v18, v18
	v_mul_f32_e32 v19, v19, v19
	v_mul_f32_e32 v20, v8, v16
	v_mul_f32_e32 v24, v9, v16
	v_mul_f32_e32 v21, v8, v17
	v_mul_f32_e32 v25, v9, v17
	v_mul_f32_e32 v22, v8, v18
	v_mul_f32_e32 v26, v9, v18
	v_mul_f32_e32 v23, v8, v19
	v_mul_f32_e32 v27, v9, v19
	v_exp_f32_e32 v20, v20
	v_exp_f32_e32 v21, v21
	v_exp_f32_e32 v22, v22
	v_exp_f32_e32 v23, v23
	v_exp_f32_e32 v24, v24
	v_exp_f32_e32 v25, v25
	v_exp_f32_e32 v26, v26
	v_exp_f32_e32 v27, v27
	v_cvt_pk_f16_f32 v38, v20, v21
	v_cvt_pk_f16_f32 v39, v22, v23
	v_cvt_pk_f16_f32 v70, v24, v25
	v_cvt_pk_f16_f32 v71, v26, v27
	v_add_u32_e32 v6, 0x8000, v6
	global_load_dwordx4 v[160:163], v6, s[12:13] offset:0 nt
	global_load_dwordx4 v[164:167], v6, s[12:13] offset:1024 nt
	global_load_dwordx4 v[168:171], v6, s[12:13] offset:2048 nt
	global_load_dwordx4 v[172:175], v6, s[12:13] offset:3072 nt
	v_add_f32_e32 v16, 0x42800000, v12
	v_add_f32_e32 v17, 0x42820000, v12
	v_add_f32_e32 v18, 0x42840000, v12
	v_add_f32_e32 v19, 0x42860000, v12
	v_mul_f32_e32 v16, v16, v16
	v_mul_f32_e32 v17, v17, v17
	v_mul_f32_e32 v18, v18, v18
	v_mul_f32_e32 v19, v19, v19
	v_mul_f32_e32 v20, v8, v16
	v_mul_f32_e32 v24, v9, v16
	v_mul_f32_e32 v21, v8, v17
	v_mul_f32_e32 v25, v9, v17
	v_mul_f32_e32 v22, v8, v18
	v_mul_f32_e32 v26, v9, v18
	v_mul_f32_e32 v23, v8, v19
	v_mul_f32_e32 v27, v9, v19
	v_exp_f32_e32 v20, v20
	v_exp_f32_e32 v21, v21
	v_exp_f32_e32 v22, v22
	v_exp_f32_e32 v23, v23
	v_exp_f32_e32 v24, v24
	v_exp_f32_e32 v25, v25
	v_exp_f32_e32 v26, v26
	v_exp_f32_e32 v27, v27
	v_cvt_pk_f16_f32 v40, v20, v21
	v_cvt_pk_f16_f32 v41, v22, v23
	v_cvt_pk_f16_f32 v72, v24, v25
	v_cvt_pk_f16_f32 v73, v26, v27
	v_add_f32_e32 v16, 0x42880000, v12
	v_add_f32_e32 v17, 0x428a0000, v12
	v_add_f32_e32 v18, 0x428c0000, v12
	v_add_f32_e32 v19, 0x428e0000, v12
	v_mul_f32_e32 v16, v16, v16
	v_mul_f32_e32 v17, v17, v17
	v_mul_f32_e32 v18, v18, v18
	v_mul_f32_e32 v19, v19, v19
	v_mul_f32_e32 v20, v8, v16
	v_mul_f32_e32 v24, v9, v16
	v_mul_f32_e32 v21, v8, v17
	v_mul_f32_e32 v25, v9, v17
	v_mul_f32_e32 v22, v8, v18
	v_mul_f32_e32 v26, v9, v18
	v_mul_f32_e32 v23, v8, v19
	v_mul_f32_e32 v27, v9, v19
	v_exp_f32_e32 v20, v20
	v_exp_f32_e32 v21, v21
	v_exp_f32_e32 v22, v22
	v_exp_f32_e32 v23, v23
	v_exp_f32_e32 v24, v24
	v_exp_f32_e32 v25, v25
	v_exp_f32_e32 v26, v26
	v_exp_f32_e32 v27, v27
	v_cvt_pk_f16_f32 v42, v20, v21
	v_cvt_pk_f16_f32 v43, v22, v23
	v_cvt_pk_f16_f32 v74, v24, v25
	v_cvt_pk_f16_f32 v75, v26, v27
	v_add_f32_e32 v16, 0x42c00000, v12
	v_add_f32_e32 v17, 0x42c20000, v12
	v_add_f32_e32 v18, 0x42c40000, v12
	v_add_f32_e32 v19, 0x42c60000, v12
	v_mul_f32_e32 v16, v16, v16
	v_mul_f32_e32 v17, v17, v17
	v_mul_f32_e32 v18, v18, v18
	v_mul_f32_e32 v19, v19, v19
	v_mul_f32_e32 v20, v8, v16
	v_mul_f32_e32 v24, v9, v16
	v_mul_f32_e32 v21, v8, v17
	v_mul_f32_e32 v25, v9, v17
	v_mul_f32_e32 v22, v8, v18
	v_mul_f32_e32 v26, v9, v18
	v_mul_f32_e32 v23, v8, v19
	v_mul_f32_e32 v27, v9, v19
	v_exp_f32_e32 v20, v20
	v_exp_f32_e32 v21, v21
	v_exp_f32_e32 v22, v22
	v_exp_f32_e32 v23, v23
	v_exp_f32_e32 v24, v24
	v_exp_f32_e32 v25, v25
	v_exp_f32_e32 v26, v26
	v_exp_f32_e32 v27, v27
	v_cvt_pk_f16_f32 v44, v20, v21
	v_cvt_pk_f16_f32 v45, v22, v23
	v_cvt_pk_f16_f32 v76, v24, v25
	v_cvt_pk_f16_f32 v77, v26, v27
	v_add_f32_e32 v16, 0x42c80000, v12
	v_add_f32_e32 v17, 0x42ca0000, v12
	v_add_f32_e32 v18, 0x42cc0000, v12
	v_add_f32_e32 v19, 0x42ce0000, v12
	v_mul_f32_e32 v16, v16, v16
	v_mul_f32_e32 v17, v17, v17
	v_mul_f32_e32 v18, v18, v18
	v_mul_f32_e32 v19, v19, v19
	v_mul_f32_e32 v20, v8, v16
	v_mul_f32_e32 v24, v9, v16
	v_mul_f32_e32 v21, v8, v17
	v_mul_f32_e32 v25, v9, v17
	v_mul_f32_e32 v22, v8, v18
	v_mul_f32_e32 v26, v9, v18
	v_mul_f32_e32 v23, v8, v19
	v_mul_f32_e32 v27, v9, v19
	v_exp_f32_e32 v20, v20
	v_exp_f32_e32 v21, v21
	v_exp_f32_e32 v22, v22
	v_exp_f32_e32 v23, v23
	v_exp_f32_e32 v24, v24
	v_exp_f32_e32 v25, v25
	v_exp_f32_e32 v26, v26
	v_exp_f32_e32 v27, v27
	v_cvt_pk_f16_f32 v46, v20, v21
	v_cvt_pk_f16_f32 v47, v22, v23
	v_cvt_pk_f16_f32 v78, v24, v25
	v_cvt_pk_f16_f32 v79, v26, v27
	v_add_u32_e32 v6, 0x8000, v6
	global_load_dwordx4 v[176:179], v6, s[12:13] offset:0 nt
	global_load_dwordx4 v[180:183], v6, s[12:13] offset:1024 nt
	global_load_dwordx4 v[184:187], v6, s[12:13] offset:2048 nt
	global_load_dwordx4 v[188:191], v6, s[12:13] offset:3072 nt
	v_mul_f32_e32 v16, v2, v2
	v_add_f32_e32 v17, 0x3f800000, v2
	v_add_f32_e32 v18, 0x40000000, v2
	v_add_f32_e32 v19, 0x40400000, v2
	v_mul_f32_e32 v17, v17, v17
	v_mul_f32_e32 v18, v18, v18
	v_mul_f32_e32 v19, v19, v19
	v_mul_f32_e32 v20, v28, v16
	v_mul_f32_e32 v24, v29, v16
	v_mul_f32_e32 v21, v28, v17
	v_mul_f32_e32 v25, v29, v17
	v_mul_f32_e32 v22, v28, v18
	v_mul_f32_e32 v26, v29, v18
	v_mul_f32_e32 v23, v28, v19
	v_mul_f32_e32 v27, v29, v19
	v_exp_f32_e32 v20, v20
	v_exp_f32_e32 v21, v21
	v_exp_f32_e32 v22, v22
	v_exp_f32_e32 v23, v23
	v_exp_f32_e32 v24, v24
	v_exp_f32_e32 v25, v25
	v_exp_f32_e32 v26, v26
	v_exp_f32_e32 v27, v27
	v_cvt_pk_f16_f32 v48, v20, v21
	v_cvt_pk_f16_f32 v49, v22, v23
	v_cvt_pk_f16_f32 v80, v24, v25
	v_cvt_pk_f16_f32 v81, v26, v27
	v_add_f32_e32 v16, 0x40800000, v2
	v_add_f32_e32 v17, 0x40a00000, v2
	v_add_f32_e32 v18, 0x40c00000, v2
	v_add_f32_e32 v19, 0x40e00000, v2
	v_mul_f32_e32 v16, v16, v16
	v_mul_f32_e32 v17, v17, v17
	v_mul_f32_e32 v18, v18, v18
	v_mul_f32_e32 v19, v19, v19
	v_mul_f32_e32 v20, v28, v16
	v_mul_f32_e32 v24, v29, v16
	v_mul_f32_e32 v21, v28, v17
	v_mul_f32_e32 v25, v29, v17
	v_mul_f32_e32 v22, v28, v18
	v_mul_f32_e32 v26, v29, v18
	v_mul_f32_e32 v23, v28, v19
	v_mul_f32_e32 v27, v29, v19
	v_exp_f32_e32 v20, v20
	v_exp_f32_e32 v21, v21
	v_exp_f32_e32 v22, v22
	v_exp_f32_e32 v23, v23
	v_exp_f32_e32 v24, v24
	v_exp_f32_e32 v25, v25
	v_exp_f32_e32 v26, v26
	v_exp_f32_e32 v27, v27
	v_cvt_pk_f16_f32 v50, v20, v21
	v_cvt_pk_f16_f32 v51, v22, v23
	v_cvt_pk_f16_f32 v82, v24, v25
	v_cvt_pk_f16_f32 v83, v26, v27
	v_add_f32_e32 v16, 0x42000000, v2
	v_add_f32_e32 v17, 0x42040000, v2
	v_add_f32_e32 v18, 0x42080000, v2
	v_add_f32_e32 v19, 0x420c0000, v2
	v_mul_f32_e32 v16, v16, v16
	v_mul_f32_e32 v17, v17, v17
	v_mul_f32_e32 v18, v18, v18
	v_mul_f32_e32 v19, v19, v19
	v_mul_f32_e32 v20, v28, v16
	v_mul_f32_e32 v24, v29, v16
	v_mul_f32_e32 v21, v28, v17
	v_mul_f32_e32 v25, v29, v17
	v_mul_f32_e32 v22, v28, v18
	v_mul_f32_e32 v26, v29, v18
	v_mul_f32_e32 v23, v28, v19
	v_mul_f32_e32 v27, v29, v19
	v_exp_f32_e32 v20, v20
	v_exp_f32_e32 v21, v21
	v_exp_f32_e32 v22, v22
	v_exp_f32_e32 v23, v23
	v_exp_f32_e32 v24, v24
	v_exp_f32_e32 v25, v25
	v_exp_f32_e32 v26, v26
	v_exp_f32_e32 v27, v27
	v_cvt_pk_f16_f32 v52, v20, v21
	v_cvt_pk_f16_f32 v53, v22, v23
	v_cvt_pk_f16_f32 v84, v24, v25
	v_cvt_pk_f16_f32 v85, v26, v27
	v_add_f32_e32 v16, 0x42100000, v2
	v_add_f32_e32 v17, 0x42140000, v2
	v_add_f32_e32 v18, 0x42180000, v2
	v_add_f32_e32 v19, 0x421c0000, v2
	v_mul_f32_e32 v16, v16, v16
	v_mul_f32_e32 v17, v17, v17
	v_mul_f32_e32 v18, v18, v18
	v_mul_f32_e32 v19, v19, v19
	v_mul_f32_e32 v20, v28, v16
	v_mul_f32_e32 v24, v29, v16
	v_mul_f32_e32 v21, v28, v17
	v_mul_f32_e32 v25, v29, v17
	v_mul_f32_e32 v22, v28, v18
	v_mul_f32_e32 v26, v29, v18
	v_mul_f32_e32 v23, v28, v19
	v_mul_f32_e32 v27, v29, v19
	v_exp_f32_e32 v20, v20
	v_exp_f32_e32 v21, v21
	v_exp_f32_e32 v22, v22
	v_exp_f32_e32 v23, v23
	v_exp_f32_e32 v24, v24
	v_exp_f32_e32 v25, v25
	v_exp_f32_e32 v26, v26
	v_exp_f32_e32 v27, v27
	v_cvt_pk_f16_f32 v54, v20, v21
	v_cvt_pk_f16_f32 v55, v22, v23
	v_cvt_pk_f16_f32 v86, v24, v25
	v_cvt_pk_f16_f32 v87, v26, v27
	v_add_u32_e32 v6, 0x8000, v6
	global_load_dwordx4 v[192:195], v6, s[12:13] offset:0 nt
	global_load_dwordx4 v[196:199], v6, s[12:13] offset:1024 nt
	global_load_dwordx4 v[200:203], v6, s[12:13] offset:2048 nt
	global_load_dwordx4 v[204:207], v6, s[12:13] offset:3072 nt
	v_add_f32_e32 v16, 0x42800000, v2
	v_add_f32_e32 v17, 0x42820000, v2
	v_add_f32_e32 v18, 0x42840000, v2
	v_add_f32_e32 v19, 0x42860000, v2
	v_mul_f32_e32 v16, v16, v16
	v_mul_f32_e32 v17, v17, v17
	v_mul_f32_e32 v18, v18, v18
	v_mul_f32_e32 v19, v19, v19
	v_mul_f32_e32 v20, v28, v16
	v_mul_f32_e32 v24, v29, v16
	v_mul_f32_e32 v21, v28, v17
	v_mul_f32_e32 v25, v29, v17
	v_mul_f32_e32 v22, v28, v18
	v_mul_f32_e32 v26, v29, v18
	v_mul_f32_e32 v23, v28, v19
	v_mul_f32_e32 v27, v29, v19
	v_exp_f32_e32 v20, v20
	v_exp_f32_e32 v21, v21
	v_exp_f32_e32 v22, v22
	v_exp_f32_e32 v23, v23
	v_exp_f32_e32 v24, v24
	v_exp_f32_e32 v25, v25
	v_exp_f32_e32 v26, v26
	v_exp_f32_e32 v27, v27
	v_cvt_pk_f16_f32 v56, v20, v21
	v_cvt_pk_f16_f32 v57, v22, v23
	v_cvt_pk_f16_f32 v88, v24, v25
	v_cvt_pk_f16_f32 v89, v26, v27
	v_add_f32_e32 v16, 0x42880000, v2
	v_add_f32_e32 v17, 0x428a0000, v2
	v_add_f32_e32 v18, 0x428c0000, v2
	v_add_f32_e32 v19, 0x428e0000, v2
	v_mul_f32_e32 v16, v16, v16
	v_mul_f32_e32 v17, v17, v17
	v_mul_f32_e32 v18, v18, v18
	v_mul_f32_e32 v19, v19, v19
	v_mul_f32_e32 v20, v28, v16
	v_mul_f32_e32 v24, v29, v16
	v_mul_f32_e32 v21, v28, v17
	v_mul_f32_e32 v25, v29, v17
	v_mul_f32_e32 v22, v28, v18
	v_mul_f32_e32 v26, v29, v18
	v_mul_f32_e32 v23, v28, v19
	v_mul_f32_e32 v27, v29, v19
	v_exp_f32_e32 v20, v20
	v_exp_f32_e32 v21, v21
	v_exp_f32_e32 v22, v22
	v_exp_f32_e32 v23, v23
	v_exp_f32_e32 v24, v24
	v_exp_f32_e32 v25, v25
	v_exp_f32_e32 v26, v26
	v_exp_f32_e32 v27, v27
	v_cvt_pk_f16_f32 v58, v20, v21
	v_cvt_pk_f16_f32 v59, v22, v23
	v_cvt_pk_f16_f32 v90, v24, v25
	v_cvt_pk_f16_f32 v91, v26, v27
	v_add_f32_e32 v16, 0x42c00000, v2
	v_add_f32_e32 v17, 0x42c20000, v2
	v_add_f32_e32 v18, 0x42c40000, v2
	v_add_f32_e32 v19, 0x42c60000, v2
	v_mul_f32_e32 v16, v16, v16
	v_mul_f32_e32 v17, v17, v17
	v_mul_f32_e32 v18, v18, v18
	v_mul_f32_e32 v19, v19, v19
	v_mul_f32_e32 v20, v28, v16
	v_mul_f32_e32 v24, v29, v16
	v_mul_f32_e32 v21, v28, v17
	v_mul_f32_e32 v25, v29, v17
	v_mul_f32_e32 v22, v28, v18
	v_mul_f32_e32 v26, v29, v18
	v_mul_f32_e32 v23, v28, v19
	v_mul_f32_e32 v27, v29, v19
	v_exp_f32_e32 v20, v20
	v_exp_f32_e32 v21, v21
	v_exp_f32_e32 v22, v22
	v_exp_f32_e32 v23, v23
	v_exp_f32_e32 v24, v24
	v_exp_f32_e32 v25, v25
	v_exp_f32_e32 v26, v26
	v_exp_f32_e32 v27, v27
	v_cvt_pk_f16_f32 v60, v20, v21
	v_cvt_pk_f16_f32 v61, v22, v23
	v_cvt_pk_f16_f32 v92, v24, v25
	v_cvt_pk_f16_f32 v93, v26, v27
	v_add_f32_e32 v16, 0x42c80000, v2
	v_add_f32_e32 v17, 0x42ca0000, v2
	v_add_f32_e32 v18, 0x42cc0000, v2
	v_add_f32_e32 v19, 0x42ce0000, v2
	v_mul_f32_e32 v16, v16, v16
	v_mul_f32_e32 v17, v17, v17
	v_mul_f32_e32 v18, v18, v18
	v_mul_f32_e32 v19, v19, v19
	v_mul_f32_e32 v20, v28, v16
	v_mul_f32_e32 v24, v29, v16
	v_mul_f32_e32 v21, v28, v17
	v_mul_f32_e32 v25, v29, v17
	v_mul_f32_e32 v22, v28, v18
	v_mul_f32_e32 v26, v29, v18
	v_mul_f32_e32 v23, v28, v19
	v_mul_f32_e32 v27, v29, v19
	v_exp_f32_e32 v20, v20
	v_exp_f32_e32 v21, v21
	v_exp_f32_e32 v22, v22
	v_exp_f32_e32 v23, v23
	v_exp_f32_e32 v24, v24
	v_exp_f32_e32 v25, v25
	v_exp_f32_e32 v26, v26
	v_exp_f32_e32 v27, v27
	v_cvt_pk_f16_f32 v62, v20, v21
	v_cvt_pk_f16_f32 v63, v22, v23
	v_cvt_pk_f16_f32 v94, v24, v25
	v_cvt_pk_f16_f32 v95, v26, v27
	v_add_u32_e32 v6, 0x8000, v6
	global_load_dwordx4 v[208:211], v6, s[12:13] offset:0 nt
	global_load_dwordx4 v[212:215], v6, s[12:13] offset:1024 nt
	global_load_dwordx4 v[216:219], v6, s[12:13] offset:2048 nt
	global_load_dwordx4 v[220:223], v6, s[12:13] offset:3072 nt
	v_mul_f32_e32 v16, v13, v13
	v_add_f32_e32 v17, 0x3f800000, v13
	v_add_f32_e32 v18, 0x40000000, v13
	v_add_f32_e32 v19, 0x40400000, v13
	v_mul_f32_e32 v17, v17, v17
	v_mul_f32_e32 v18, v18, v18
	v_mul_f32_e32 v19, v19, v19
	v_mul_f32_e32 v20, v8, v16
	v_mul_f32_e32 v24, v9, v16
	v_mul_f32_e32 v21, v8, v17
	v_mul_f32_e32 v25, v9, v17
	v_mul_f32_e32 v22, v8, v18
	v_mul_f32_e32 v26, v9, v18
	v_mul_f32_e32 v23, v8, v19
	v_mul_f32_e32 v27, v9, v19
	v_exp_f32_e32 v20, v20
	v_exp_f32_e32 v21, v21
	v_exp_f32_e32 v22, v22
	v_exp_f32_e32 v23, v23
	v_exp_f32_e32 v24, v24
	v_exp_f32_e32 v25, v25
	v_exp_f32_e32 v26, v26
	v_exp_f32_e32 v27, v27
	v_mul_f32_e32 v96, v10, v20
	v_mul_f32_e32 v97, v10, v21
	v_mul_f32_e32 v98, v10, v22
	v_mul_f32_e32 v99, v10, v23
	v_mul_f32_e32 v112, v11, v24
	v_mul_f32_e32 v113, v11, v25
	v_mul_f32_e32 v114, v11, v26
	v_mul_f32_e32 v115, v11, v27
	v_mul_f32_e32 v16, v3, v3
	v_add_f32_e32 v17, 0x3f800000, v3
	v_add_f32_e32 v18, 0x40000000, v3
	v_add_f32_e32 v19, 0x40400000, v3
	v_mul_f32_e32 v17, v17, v17
	v_mul_f32_e32 v18, v18, v18
	v_mul_f32_e32 v19, v19, v19
	v_mul_f32_e32 v20, v28, v16
	v_mul_f32_e32 v24, v29, v16
	v_mul_f32_e32 v21, v28, v17
	v_mul_f32_e32 v25, v29, v17
	v_mul_f32_e32 v22, v28, v18
	v_mul_f32_e32 v26, v29, v18
	v_mul_f32_e32 v23, v28, v19
	v_mul_f32_e32 v27, v29, v19
	v_exp_f32_e32 v20, v20
	v_exp_f32_e32 v21, v21
	v_exp_f32_e32 v22, v22
	v_exp_f32_e32 v23, v23
	v_exp_f32_e32 v24, v24
	v_exp_f32_e32 v25, v25
	v_exp_f32_e32 v26, v26
	v_exp_f32_e32 v27, v27
	v_mul_f32_e32 v104, v30, v20
	v_mul_f32_e32 v105, v30, v21
	v_mul_f32_e32 v106, v30, v22
	v_mul_f32_e32 v107, v30, v23
	v_mul_f32_e32 v120, v31, v24
	v_mul_f32_e32 v121, v31, v25
	v_mul_f32_e32 v122, v31, v26
	v_mul_f32_e32 v123, v31, v27
	s_waitcnt vmcnt(20)
	v_add_f32_e32 v128, v128, v129
	v_add_f32_e32 v130, v130, v131
	v_add_f32_e32 v132, v132, v133
	v_add_f32_e32 v134, v134, v135
	v_add_f32_e32 v136, v136, v137
	v_add_f32_e32 v138, v138, v139
	v_add_f32_e32 v140, v140, v141
	v_add_f32_e32 v142, v142, v143
	v_add_f32_e32 v128, v128, v130
	v_add_f32_e32 v132, v132, v134
	v_add_f32_e32 v136, v136, v138
	v_add_f32_e32 v140, v140, v142
	v_cndmask_b32_e64 v130, v128, v132, s[30:31]
	v_cndmask_b32_e64 v134, v136, v140, s[30:31]
	v_cndmask_b32_e64 v129, v132, v128, s[30:31]
	v_cndmask_b32_e64 v133, v140, v136, s[30:31]
	v_add_f32_dpp v129, v130, v129 quad_perm:[1,0,3,2] row_mask:0xf bank_mask:0xf bound_ctrl:1
	v_add_f32_dpp v133, v134, v133 quad_perm:[1,0,3,2] row_mask:0xf bank_mask:0xf bound_ctrl:1
	v_cndmask_b32_e64 v135, v129, v133, s[32:33]
	v_cndmask_b32_e64 v131, v133, v129, s[32:33]
	s_nop 1
	v_add_f32_dpp v131, v135, v131 quad_perm:[2,3,0,1] row_mask:0xf bank_mask:0xf bound_ctrl:1
	v_cvt_f16_f32_e32 v131, v131
	ds_write_b16 v14, v131 offset:0
	s_waitcnt vmcnt(16)
	v_add_f32_e32 v144, v144, v145
	v_add_f32_e32 v146, v146, v147
	v_add_f32_e32 v148, v148, v149
	v_add_f32_e32 v150, v150, v151
	v_add_f32_e32 v152, v152, v153
	v_add_f32_e32 v154, v154, v155
	v_add_f32_e32 v156, v156, v157
	v_add_f32_e32 v158, v158, v159
	v_add_f32_e32 v144, v144, v146
	v_add_f32_e32 v148, v148, v150
	v_add_f32_e32 v152, v152, v154
	v_add_f32_e32 v156, v156, v158
	v_cndmask_b32_e64 v146, v144, v148, s[30:31]
	v_cndmask_b32_e64 v150, v152, v156, s[30:31]
	v_cndmask_b32_e64 v145, v148, v144, s[30:31]
	v_cndmask_b32_e64 v149, v156, v152, s[30:31]
	v_add_f32_dpp v145, v146, v145 quad_perm:[1,0,3,2] row_mask:0xf bank_mask:0xf bound_ctrl:1
	v_add_f32_dpp v149, v150, v149 quad_perm:[1,0,3,2] row_mask:0xf bank_mask:0xf bound_ctrl:1
	v_cndmask_b32_e64 v151, v145, v149, s[32:33]
	v_cndmask_b32_e64 v147, v149, v145, s[32:33]
	s_nop 1
	v_add_f32_dpp v147, v151, v147 quad_perm:[2,3,0,1] row_mask:0xf bank_mask:0xf bound_ctrl:1
	v_cvt_f16_f32_e32 v147, v147
	ds_write_b16 v14, v147 offset:1088
	s_waitcnt vmcnt(12)
	v_add_f32_e32 v160, v160, v161
	v_add_f32_e32 v162, v162, v163
	v_add_f32_e32 v164, v164, v165
	v_add_f32_e32 v166, v166, v167
	v_add_f32_e32 v168, v168, v169
	v_add_f32_e32 v170, v170, v171
	v_add_f32_e32 v172, v172, v173
	v_add_f32_e32 v174, v174, v175
	v_add_f32_e32 v160, v160, v162
	v_add_f32_e32 v164, v164, v166
	v_add_f32_e32 v168, v168, v170
	v_add_f32_e32 v172, v172, v174
	v_cndmask_b32_e64 v162, v160, v164, s[30:31]
	v_cndmask_b32_e64 v166, v168, v172, s[30:31]
	v_cndmask_b32_e64 v161, v164, v160, s[30:31]
	v_cndmask_b32_e64 v165, v172, v168, s[30:31]
	v_add_f32_dpp v161, v162, v161 quad_perm:[1,0,3,2] row_mask:0xf bank_mask:0xf bound_ctrl:1
	v_add_f32_dpp v165, v166, v165 quad_perm:[1,0,3,2] row_mask:0xf bank_mask:0xf bound_ctrl:1
	v_cndmask_b32_e64 v167, v161, v165, s[32:33]
	v_cndmask_b32_e64 v163, v165, v161, s[32:33]
	s_nop 1
	v_add_f32_dpp v163, v167, v163 quad_perm:[2,3,0,1] row_mask:0xf bank_mask:0xf bound_ctrl:1
	v_cvt_f16_f32_e32 v163, v163
	ds_write_b16 v14, v163 offset:2176
	s_waitcnt vmcnt(8)
	v_add_f32_e32 v176, v176, v177
	v_add_f32_e32 v178, v178, v179
	v_add_f32_e32 v180, v180, v181
	v_add_f32_e32 v182, v182, v183
	v_add_f32_e32 v184, v184, v185
	v_add_f32_e32 v186, v186, v187
	v_add_f32_e32 v188, v188, v189
	v_add_f32_e32 v190, v190, v191
	v_add_f32_e32 v176, v176, v178
	v_add_f32_e32 v180, v180, v182
	v_add_f32_e32 v184, v184, v186
	v_add_f32_e32 v188, v188, v190
	v_cndmask_b32_e64 v178, v176, v180, s[30:31]
	v_cndmask_b32_e64 v182, v184, v188, s[30:31]
	v_cndmask_b32_e64 v177, v180, v176, s[30:31]
	v_cndmask_b32_e64 v181, v188, v184, s[30:31]
	v_add_f32_dpp v177, v178, v177 quad_perm:[1,0,3,2] row_mask:0xf bank_mask:0xf bound_ctrl:1
	v_add_f32_dpp v181, v182, v181 quad_perm:[1,0,3,2] row_mask:0xf bank_mask:0xf bound_ctrl:1
	v_cndmask_b32_e64 v183, v177, v181, s[32:33]
	v_cndmask_b32_e64 v179, v181, v177, s[32:33]
	s_nop 1
	v_add_f32_dpp v179, v183, v179 quad_perm:[2,3,0,1] row_mask:0xf bank_mask:0xf bound_ctrl:1
	v_cvt_f16_f32_e32 v179, v179
	ds_write_b16 v14, v179 offset:3264
	s_mov_b32 s29, 0
	v_mov_b32_e32 v160, 0
	v_mov_b32_e32 v161, 0
	v_mov_b32_e32 v162, 0
	v_mov_b32_e32 v163, 0
	s_lshl_b32 s6, s6, 6
	s_add_i32 s6, s6, s7
	s_lshl_b32 s6, s6, 10
	v_add_u32_e32 v5, s6, v5
	s_branch .Lpass
.Lsecond_half:
	v_add_f32_e32 v16, 0x41800000, v13
	v_add_f32_e32 v17, 0x41880000, v13
	v_add_f32_e32 v18, 0x41900000, v13
	v_add_f32_e32 v19, 0x41980000, v13
	v_mul_f32_e32 v16, v16, v16
	v_mul_f32_e32 v17, v17, v17
	v_mul_f32_e32 v18, v18, v18
	v_mul_f32_e32 v19, v19, v19
	v_mul_f32_e32 v20, v8, v16
	v_mul_f32_e32 v24, v9, v16
	v_mul_f32_e32 v21, v8, v17
	v_mul_f32_e32 v25, v9, v17
	v_mul_f32_e32 v22, v8, v18
	v_mul_f32_e32 v26, v9, v18
	v_mul_f32_e32 v23, v8, v19
	v_mul_f32_e32 v27, v9, v19
	v_exp_f32_e32 v20, v20
	v_exp_f32_e32 v21, v21
	v_exp_f32_e32 v22, v22
	v_exp_f32_e32 v23, v23
	v_exp_f32_e32 v24, v24
	v_exp_f32_e32 v25, v25
	v_exp_f32_e32 v26, v26
	v_exp_f32_e32 v27, v27
	v_mul_f32_e32 v96, v10, v20
	v_mul_f32_e32 v97, v10, v21
	v_mul_f32_e32 v98, v10, v22
	v_mul_f32_e32 v99, v10, v23
	v_mul_f32_e32 v112, v11, v24
	v_mul_f32_e32 v113, v11, v25
	v_mul_f32_e32 v114, v11, v26
	v_mul_f32_e32 v115, v11, v27
	v_add_f32_e32 v16, 0x41800000, v3
	v_add_f32_e32 v17, 0x41880000, v3
	v_add_f32_e32 v18, 0x41900000, v3
	v_add_f32_e32 v19, 0x41980000, v3
	v_mul_f32_e32 v16, v16, v16
	v_mul_f32_e32 v17, v17, v17
	v_mul_f32_e32 v18, v18, v18
	v_mul_f32_e32 v19, v19, v19
	v_mul_f32_e32 v20, v28, v16
	v_mul_f32_e32 v24, v29, v16
	v_mul_f32_e32 v21, v28, v17
	v_mul_f32_e32 v25, v29, v17
	v_mul_f32_e32 v22, v28, v18
	v_mul_f32_e32 v26, v29, v18
	v_mul_f32_e32 v23, v28, v19
	v_mul_f32_e32 v27, v29, v19
	v_exp_f32_e32 v20, v20
	v_exp_f32_e32 v21, v21
	v_exp_f32_e32 v22, v22
	v_exp_f32_e32 v23, v23
	v_exp_f32_e32 v24, v24
	v_exp_f32_e32 v25, v25
	v_exp_f32_e32 v26, v26
	v_exp_f32_e32 v27, v27
	v_mul_f32_e32 v104, v30, v20
	v_mul_f32_e32 v105, v30, v21
	v_mul_f32_e32 v106, v30, v22
	v_mul_f32_e32 v107, v30, v23
	v_mul_f32_e32 v120, v31, v24
	v_mul_f32_e32 v121, v31, v25
	v_mul_f32_e32 v122, v31, v26
	v_mul_f32_e32 v123, v31, v27
	v_add_u32_e32 v6, 0x8000, v6
	global_load_dwordx4 v[224:227], v6, s[12:13] offset:0 nt
	global_load_dwordx4 v[228:231], v6, s[12:13] offset:1024 nt
	global_load_dwordx4 v[232:235], v6, s[12:13] offset:2048 nt
	global_load_dwordx4 v[236:239], v6, s[12:13] offset:3072 nt
	v_add_u32_e32 v6, 0x8000, v6
	global_load_dwordx4 v[240:243], v6, s[12:13] offset:0 nt
	global_load_dwordx4 v[244:247], v6, s[12:13] offset:1024 nt
	global_load_dwordx4 v[248:251], v6, s[12:13] offset:2048 nt
	global_load_dwordx4 v[252:255], v6, s[12:13] offset:3072 nt
	s_waitcnt vmcnt(12)
	v_add_f32_e32 v192, v192, v193
	v_add_f32_e32 v194, v194, v195
	v_add_f32_e32 v196, v196, v197
	v_add_f32_e32 v198, v198, v199
	v_add_f32_e32 v200, v200, v201
	v_add_f32_e32 v202, v202, v203
	v_add_f32_e32 v204, v204, v205
	v_add_f32_e32 v206, v206, v207
	v_add_f32_e32 v192, v192, v194
	v_add_f32_e32 v196, v196, v198
	v_add_f32_e32 v200, v200, v202
	v_add_f32_e32 v204, v204, v206
	v_cndmask_b32_e64 v194, v192, v196, s[30:31]
	v_cndmask_b32_e64 v198, v200, v204, s[30:31]
	v_cndmask_b32_e64 v193, v196, v192, s[30:31]
	v_cndmask_b32_e64 v197, v204, v200, s[30:31]
	v_add_f32_dpp v193, v194, v193 quad_perm:[1,0,3,2] row_mask:0xf bank_mask:0xf bound_ctrl:1
	v_add_f32_dpp v197, v198, v197 quad_perm:[1,0,3,2] row_mask:0xf bank_mask:0xf bound_ctrl:1
	v_cndmask_b32_e64 v199, v193, v197, s[32:33]
	v_cndmask_b32_e64 v195, v197, v193, s[32:33]
	s_nop 1
	v_add_f32_dpp v195, v199, v195 quad_perm:[2,3,0,1] row_mask:0xf bank_mask:0xf bound_ctrl:1
	v_cvt_f16_f32_e32 v195, v195
	ds_write_b16 v14, v195 offset:4352
	s_waitcnt vmcnt(8)
	v_add_f32_e32 v208, v208, v209
	v_add_f32_e32 v210, v210, v211
	v_add_f32_e32 v212, v212, v213
	v_add_f32_e32 v214, v214, v215
	v_add_f32_e32 v216, v216, v217
	v_add_f32_e32 v218, v218, v219
	v_add_f32_e32 v220, v220, v221
	v_add_f32_e32 v222, v222, v223
	v_add_f32_e32 v208, v208, v210
	v_add_f32_e32 v212, v212, v214
	v_add_f32_e32 v216, v216, v218
	v_add_f32_e32 v220, v220, v222
	v_cndmask_b32_e64 v210, v208, v212, s[30:31]
	v_cndmask_b32_e64 v214, v216, v220, s[30:31]
	v_cndmask_b32_e64 v209, v212, v208, s[30:31]
	v_cndmask_b32_e64 v213, v220, v216, s[30:31]
	v_add_f32_dpp v209, v210, v209 quad_perm:[1,0,3,2] row_mask:0xf bank_mask:0xf bound_ctrl:1
	v_add_f32_dpp v213, v214, v213 quad_perm:[1,0,3,2] row_mask:0xf bank_mask:0xf bound_ctrl:1
	v_cndmask_b32_e64 v215, v209, v213, s[32:33]
	v_cndmask_b32_e64 v211, v213, v209, s[32:33]
	s_nop 1
	v_add_f32_dpp v211, v215, v211 quad_perm:[2,3,0,1] row_mask:0xf bank_mask:0xf bound_ctrl:1
	v_cvt_f16_f32_e32 v211, v211
	ds_write_b16 v14, v211 offset:5440
	s_waitcnt vmcnt(4)
	v_add_f32_e32 v224, v224, v225
	v_add_f32_e32 v226, v226, v227
	v_add_f32_e32 v228, v228, v229
	v_add_f32_e32 v230, v230, v231
	v_add_f32_e32 v232, v232, v233
	v_add_f32_e32 v234, v234, v235
	v_add_f32_e32 v236, v236, v237
	v_add_f32_e32 v238, v238, v239
	v_add_f32_e32 v224, v224, v226
	v_add_f32_e32 v228, v228, v230
	v_add_f32_e32 v232, v232, v234
	v_add_f32_e32 v236, v236, v238
	v_cndmask_b32_e64 v226, v224, v228, s[30:31]
	v_cndmask_b32_e64 v230, v232, v236, s[30:31]
	v_cndmask_b32_e64 v225, v228, v224, s[30:31]
	v_cndmask_b32_e64 v229, v236, v232, s[30:31]
	v_add_f32_dpp v225, v226, v225 quad_perm:[1,0,3,2] row_mask:0xf bank_mask:0xf bound_ctrl:1
	v_add_f32_dpp v229, v230, v229 quad_perm:[1,0,3,2] row_mask:0xf bank_mask:0xf bound_ctrl:1
	v_cndmask_b32_e64 v231, v225, v229, s[32:33]
	v_cndmask_b32_e64 v227, v229, v225, s[32:33]
	s_nop 1
	v_add_f32_dpp v227, v231, v227 quad_perm:[2,3,0,1] row_mask:0xf bank_mask:0xf bound_ctrl:1
	v_cvt_f16_f32_e32 v227, v227
	ds_write_b16 v14, v227 offset:6528
	s_waitcnt vmcnt(0)
	v_add_f32_e32 v240, v240, v241
	v_add_f32_e32 v242, v242, v243
	v_add_f32_e32 v244, v244, v245
	v_add_f32_e32 v246, v246, v247
	v_add_f32_e32 v248, v248, v249
	v_add_f32_e32 v250, v250, v251
	v_add_f32_e32 v252, v252, v253
	v_add_f32_e32 v254, v254, v255
	v_add_f32_e32 v240, v240, v242
	v_add_f32_e32 v244, v244, v246
	v_add_f32_e32 v248, v248, v250
	v_add_f32_e32 v252, v252, v254
	v_cndmask_b32_e64 v242, v240, v244, s[30:31]
	v_cndmask_b32_e64 v246, v248, v252, s[30:31]
	v_cndmask_b32_e64 v241, v244, v240, s[30:31]
	v_cndmask_b32_e64 v245, v252, v248, s[30:31]
	v_add_f32_dpp v241, v242, v241 quad_perm:[1,0,3,2] row_mask:0xf bank_mask:0xf bound_ctrl:1
	v_add_f32_dpp v245, v246, v245 quad_perm:[1,0,3,2] row_mask:0xf bank_mask:0xf bound_ctrl:1
	v_cndmask_b32_e64 v247, v241, v245, s[32:33]
	v_cndmask_b32_e64 v243, v245, v241, s[32:33]
	s_nop 1
	v_add_f32_dpp v243, v247, v243 quad_perm:[2,3,0,1] row_mask:0xf bank_mask:0xf bound_ctrl:1
	v_cvt_f16_f32_e32 v243, v243
	ds_write_b16 v14, v243 offset:7616
.Lpass:
	s_waitcnt lgkmcnt(0)
	s_barrier
	ds_read_b128 v[144:147], v15 offset:0
	ds_read_b128 v[148:151], v15 offset:64
	ds_read_b128 v[152:155], v15 offset:128
	ds_read_b128 v[156:159], v15 offset:192
	s_waitcnt lgkmcnt(3)
	v_mfma_f32_16x16x32_f16 v[128:131], v[144:147], v[32:35], 0
	v_mfma_f32_16x16x32_f16 v[136:139], v[144:147], v[64:67], 0
	v_mfma_f32_16x16x32_f16 v[132:135], v[144:147], v[48:51], 0
	v_mfma_f32_16x16x32_f16 v[140:143], v[144:147], v[80:83], 0
	s_waitcnt lgkmcnt(2)
	v_mfma_f32_16x16x32_f16 v[128:131], v[148:151], v[36:39], v[128:131]
	v_mfma_f32_16x16x32_f16 v[136:139], v[148:151], v[68:71], v[136:139]
	v_mfma_f32_16x16x32_f16 v[132:135], v[148:151], v[52:55], v[132:135]
	v_mfma_f32_16x16x32_f16 v[140:143], v[148:151], v[84:87], v[140:143]
	s_waitcnt lgkmcnt(1)
	v_mfma_f32_16x16x32_f16 v[128:131], v[152:155], v[40:43], v[128:131]
	v_mfma_f32_16x16x32_f16 v[136:139], v[152:155], v[72:75], v[136:139]
	v_mfma_f32_16x16x32_f16 v[132:135], v[152:155], v[56:59], v[132:135]
	v_mfma_f32_16x16x32_f16 v[140:143], v[152:155], v[88:91], v[140:143]
	s_waitcnt lgkmcnt(0)
	v_mfma_f32_16x16x32_f16 v[128:131], v[156:159], v[44:47], v[128:131]
	v_mfma_f32_16x16x32_f16 v[136:139], v[156:159], v[76:79], v[136:139]
	v_mfma_f32_16x16x32_f16 v[132:135], v[156:159], v[60:63], v[132:135]
	v_mfma_f32_16x16x32_f16 v[140:143], v[156:159], v[92:95], v[140:143]
	s_nop 15
	v_fma_f32 v160, v96, v128, v160
	v_fma_f32 v161, -v112, v136, v161
	v_fma_f32 v162, v104, v132, v162
	v_fma_f32 v163, -v120, v140, v163
	v_fma_f32 v160, v97, v129, v160
	v_fma_f32 v161, -v113, v137, v161
	v_fma_f32 v162, v105, v133, v162
	v_fma_f32 v163, -v121, v141, v163
	v_fma_f32 v160, v98, v130, v160
	v_fma_f32 v161, -v114, v138, v161
	v_fma_f32 v162, v106, v134, v162
	v_fma_f32 v163, -v122, v142, v163
	v_fma_f32 v160, v99, v131, v160
	v_fma_f32 v161, -v115, v139, v161
	v_fma_f32 v162, v107, v135, v162
	v_fma_f32 v163, -v123, v143, v163
	v_add_f32_e32 v164, v160, v161
	v_add_f32_e32 v165, v162, v163
	v_cmp_gt_u32_e32 vcc, 32, v1
	s_cmp_eq_u32 s29, 1
	v_permlane16_swap_b32_e32 v164, v165
	s_nop 0
	v_add_f32_e32 v164, v164, v165
	v_mov_b32_e32 v165, v164
	s_nop 1
	v_permlane32_swap_b32_e32 v164, v165
	s_nop 0
	v_add_f32_e32 v164, v164, v165
	s_cbranch_scc1 .Lstore
	s_mov_b32 s29, 1
	v_add_u32_e32 v15, 0x1100, v15
	s_branch .Lsecond_half
